# combo7 + prep unit loop: all 27 loads of a unit issued at its top (disjoint columns), b_forget kept in registers, counted waits at use
# speedup vs baseline: 1.0068x; 1.0068x over previous
.LBB0_307:
	s_or_b64 exec, exec, s[24:25]
	v_readlane_b32 s8, v254, 7
	s_mov_b32 s4, s61
	s_mov_b32 s22, s61
	v_readlane_b32 s0, v254, 3
	v_readlane_b32 s9, v254, 8
	s_waitcnt lgkmcnt(0)
	s_barrier
	v_mbcnt_lo_u32_b32 v33, -1, 0
	v_mbcnt_hi_u32_b32 v33, -1, v33
	s_load_dword s1, s[8:9], 0xb0
	s_cmpk_gt_i32 s0, 0x3ff
	s_waitcnt lgkmcnt(0)
	s_cbranch_scc1 .LBB0_324
	s_load_dwordx2 s[6:7], s[8:9], 0xa8
	s_movk_i32 s2, 0x48
	v_readlane_b32 s24, v254, 55
	v_readlane_b32 s25, v254, 56
	v_and_b32_e32 v36, 15, v33
	s_waitcnt lgkmcnt(0)
	s_add_u32 s10, s6, 0x54000000
	s_addc_u32 s11, s7, 0
	s_add_u32 s12, s6, 0x1800000
	s_addc_u32 s13, s7, 0
	s_cmp_gt_u32 s22, 3
	s_cselect_b64 s[14:15], -1, 0
	s_cmp_lt_u32 s22, 4
	s_cselect_b32 s2, s2, 0x50
	s_add_u32 s2, s8, s2
	s_addc_u32 s3, s9, 0
	s_load_dwordx2 s[2:3], s[2:3], 0x0
	s_lshl_b32 s40, s24, 13
	s_lshl_b64 s[16:17], s[40:41], 2
	v_bfe_u32 v35, v33, 4, 2
	v_lshl_or_b32 v37, s4, 6, v33
	s_waitcnt lgkmcnt(0)
	s_add_u32 s2, s2, s16
	s_addc_u32 s3, s3, s17
	s_add_u32 s16, s6, 0xe00000
	s_addc_u32 s17, s7, 0
	s_lshl_b32 s25, s22, 4
	s_and_b32 s23, s25, 16
	v_or_b32_e32 v0, s23, v36
	v_lshlrev_b32_e32 v0, 2, v0
	v_lshl_or_b32 v31, v35, 11, v0
	v_or_b32_e32 v178, 0x6000, v31
	global_load_dword v114, v178, s[2:3] offset:128
	v_or_b32_e32 v179, 0x6100, v31
	global_load_dword v115, v179, s[2:3] offset:128
	v_or_b32_e32 v180, 0x6300, v31
	global_load_dword v116, v180, s[2:3] offset:128
	v_or_b32_e32 v181, 0x6700, v31
	global_load_dword v117, v181, s[2:3] offset:128
	v_or_b32_e32 v178, 0x4700, v31
	global_load_dword v118, v178, s[2:3] offset:128
	v_or_b32_e32 v179, 0x100, v31
	global_load_dword v119, v179, s[2:3] offset:128
	v_or_b32_e32 v180, 0x300, v31
	global_load_dword v120, v180, s[2:3] offset:128
	v_or_b32_e32 v181, 0x6500, v31
	global_load_dword v121, v181, s[2:3] offset:128
	v_or_b32_e32 v178, 0x4300, v31
	global_load_dword v122, v178, s[2:3] offset:128
	v_or_b32_e32 v179, 0x2700, v31
	global_load_dword v123, v179, s[2:3] offset:128
	v_or_b32_e32 v180, 0x4100, v31
	global_load_dword v124, v180, s[2:3] offset:128
	v_or_b32_e32 v181, 0x2300, v31
	global_load_dword v125, v181, s[2:3] offset:128
	v_or_b32_e32 v178, 0x4500, v31
	global_load_dword v126, v178, s[2:3] offset:128
	v_or_b32_e32 v179, 0x2100, v31
	global_load_dword v127, v179, s[2:3] offset:128
	v_or_b32_e32 v180, 0x2500, v31
	global_load_dword v128, v180, s[2:3] offset:128
	v_or_b32_e32 v181, 0x6200, v31
	global_load_dword v129, v181, s[2:3] offset:128
	v_or_b32_e32 v178, 0x6400, v31
	global_load_dword v130, v178, s[2:3] offset:128
	v_or_b32_e32 v179, 0x6600, v31
	global_load_dword v131, v179, s[2:3] offset:128
	v_or_b32_e32 v180, 0x4000, v31
	global_load_dword v132, v180, s[2:3] offset:128
	v_or_b32_e32 v181, 0x4200, v31
	global_load_dword v133, v181, s[2:3] offset:128
	v_or_b32_e32 v178, 0x4400, v31
	global_load_dword v134, v178, s[2:3] offset:128
	v_or_b32_e32 v179, 0x4600, v31
	global_load_dword v135, v179, s[2:3] offset:128
	v_or_b32_e32 v180, 0x2000, v31
	global_load_dword v136, v180, s[2:3] offset:128
	v_or_b32_e32 v181, 0x2200, v31
	global_load_dword v137, v181, s[2:3] offset:128
	v_or_b32_e32 v178, 0x2400, v31
	global_load_dword v138, v178, s[2:3] offset:128
	v_or_b32_e32 v179, 0x2600, v31
	global_load_dword v139, v179, s[2:3] offset:128
	global_load_dword v140, v31, s[2:3] offset:128
	v_or_b32_e32 v181, 0x200, v31
	global_load_dword v141, v181, s[2:3] offset:128
	v_or_b32_e32 v178, 0x500, v31
	global_load_dword v142, v178, s[2:3] offset:128
	v_or_b32_e32 v179, 0x400, v31
	global_load_dword v143, v179, s[2:3] offset:128
	v_or_b32_e32 v180, 0x700, v31
	global_load_dword v144, v180, s[2:3] offset:128
	v_or_b32_e32 v181, 0x600, v31
	global_load_dword v145, v181, s[2:3] offset:128
	v_or_b32_e32 v178, 0x6000, v31
	global_load_dword v146, v178, s[2:3]
	v_or_b32_e32 v179, 0x6100, v31
	global_load_dword v147, v179, s[2:3]
	v_or_b32_e32 v180, 0x6200, v31
	global_load_dword v148, v180, s[2:3]
	v_or_b32_e32 v181, 0x6300, v31
	global_load_dword v149, v181, s[2:3]
	v_or_b32_e32 v178, 0x6400, v31
	global_load_dword v150, v178, s[2:3]
	v_or_b32_e32 v179, 0x6500, v31
	global_load_dword v151, v179, s[2:3]
	v_or_b32_e32 v180, 0x6600, v31
	global_load_dword v152, v180, s[2:3]
	v_or_b32_e32 v181, 0x6700, v31
	global_load_dword v153, v181, s[2:3]
	v_or_b32_e32 v178, 0x4000, v31
	global_load_dword v154, v178, s[2:3]
	v_or_b32_e32 v179, 0x4100, v31
	global_load_dword v155, v179, s[2:3]
	v_or_b32_e32 v180, 0x4200, v31
	global_load_dword v156, v180, s[2:3]
	v_or_b32_e32 v181, 0x4300, v31
	global_load_dword v157, v181, s[2:3]
	v_or_b32_e32 v178, 0x4400, v31
	global_load_dword v158, v178, s[2:3]
	v_or_b32_e32 v179, 0x4500, v31
	global_load_dword v159, v179, s[2:3]
	v_or_b32_e32 v180, 0x4600, v31
	global_load_dword v160, v180, s[2:3]
	v_or_b32_e32 v181, 0x4700, v31
	global_load_dword v161, v181, s[2:3]
	v_or_b32_e32 v178, 0x2000, v31
	global_load_dword v162, v178, s[2:3]
	v_or_b32_e32 v179, 0x2100, v31
	global_load_dword v163, v179, s[2:3]
	v_or_b32_e32 v180, 0x2200, v31
	global_load_dword v164, v180, s[2:3]
	v_or_b32_e32 v181, 0x2300, v31
	global_load_dword v165, v181, s[2:3]
	v_or_b32_e32 v178, 0x2400, v31
	global_load_dword v166, v178, s[2:3]
	v_or_b32_e32 v179, 0x2500, v31
	global_load_dword v167, v179, s[2:3]
	v_or_b32_e32 v180, 0x2600, v31
	global_load_dword v168, v180, s[2:3]
	v_or_b32_e32 v181, 0x2700, v31
	global_load_dword v169, v181, s[2:3]
	global_load_dword v170, v31, s[2:3]
	global_load_dword v171, v31, s[2:3] offset:256
	global_load_dword v172, v31, s[2:3] offset:512
	global_load_dword v173, v31, s[2:3] offset:768
	global_load_dword v174, v31, s[2:3] offset:1024
	global_load_dword v175, v31, s[2:3] offset:1280
	global_load_dword v176, v31, s[2:3] offset:1536
	global_load_dword v177, v31, s[2:3] offset:1792
	s_add_u32 s18, s6, 0x440000
	s_addc_u32 s19, s7, 0
	s_add_u32 s20, s6, 0x400000
	s_addc_u32 s21, s7, 0
	s_lshl_b32 s40, s24, 7
	s_lshl_b64 s[4:5], s[40:41], 2
	v_and_b32_e32 v34, 63, v33
	v_ashrrev_i32_e32 v96, 3, v37
	v_and_b32_e32 v37, 7, v33
	v_and_or_b32 v97, s25, 32, v36
	v_lshl_or_b32 v36, v35, 2, s23
	v_lshlrev_b32_e32 v32, 1, v34
	v_lshlrev_b32_e32 v184, 4, v37
	v_mov_b32_e32 v35, v185
	v_lshl_add_u64 v[68:69], s[18:19], 0, v[184:185]
	v_lshl_add_u64 v[66:67], s[20:21], 0, v[184:185]
	v_or_b32_e32 v99, 16, v97
	v_lshlrev_b32_e32 v84, 1, v32
	v_lshlrev_b32_e32 v39, 3, v33
	v_and_b32_e32 v40, 8, v39
	v_lshl_add_u32 v39, v34, 2, 0
	v_and_b32_e32 v33, 48, v33
	v_add_u32_e32 v33, 0, v33
	v_lshlrev_b32_e32 v82, 1, v40
	v_lshlrev_b32_e32 v42, 2, v40
	v_lshl_add_u32 v41, v97, 1, 0
	v_mov_b32_e32 v43, v185
	v_lshl_add_u64 v[42:43], s[6:7], 0, v[42:43]
	s_load_dwordx2 s[2:3], s[8:9], 0x40
	s_waitcnt lgkmcnt(0)
	s_add_u32 s2, s2, s4
	s_addc_u32 s3, s3, s5
	v_cmp_eq_u32_e64 s[4:5], 2, v37
	s_lshl_b32 s40, s24, 2
	s_lshl_b32 s24, s22, 3
	s_mulk_i32 s22, 0x880
	s_lshl_b32 s25, s0, 6
	s_lshl_b32 s26, s1, 6
	v_add_u32_e32 v100, s22, v39
	s_waitcnt vmcnt(0)
	v_cvt_pk_bf16_f32 v0, v114, v115
	v_cvt_pk_bf16_f32 v1, v129, v116
	v_cvt_pk_bf16_f32 v2, v130, v121
	v_cvt_pk_bf16_f32 v3, v131, v117
	v_cvt_pk_bf16_f32 v4, v132, v124
	v_cvt_pk_bf16_f32 v5, v133, v122
	v_cvt_pk_bf16_f32 v6, v134, v126
	v_cvt_pk_bf16_f32 v7, v135, v118
	v_cvt_pk_bf16_f32 v8, v136, v127
	v_cvt_pk_bf16_f32 v9, v137, v125
	v_cvt_pk_bf16_f32 v10, v138, v128
	v_cvt_pk_bf16_f32 v11, v139, v123
	v_cvt_pk_bf16_f32 v12, v140, v119
	v_cvt_pk_bf16_f32 v13, v141, v120
	v_cvt_pk_bf16_f32 v14, v143, v142
	v_cvt_pk_bf16_f32 v15, v145, v144
	v_cvt_pk_bf16_f32 v16, v146, v147
	v_cvt_pk_bf16_f32 v17, v148, v149
	v_cvt_pk_bf16_f32 v18, v150, v151
	v_cvt_pk_bf16_f32 v19, v152, v153
	v_cvt_pk_bf16_f32 v20, v154, v155
	v_cvt_pk_bf16_f32 v21, v156, v157
	v_cvt_pk_bf16_f32 v22, v158, v159
	v_cvt_pk_bf16_f32 v23, v160, v161
	v_cvt_pk_bf16_f32 v24, v162, v163
	v_cvt_pk_bf16_f32 v25, v164, v165
	v_cvt_pk_bf16_f32 v26, v166, v167
	v_cvt_pk_bf16_f32 v27, v168, v169
	v_cvt_pk_bf16_f32 v28, v170, v171
	v_cvt_pk_bf16_f32 v29, v172, v173
	v_cvt_pk_bf16_f32 v30, v174, v175
	v_cvt_pk_bf16_f32 v31, v176, v177
	v_lshlrev_b32_e32 v38, 3, v34
	global_load_dwordx2 v[64:65], v38, s[2:3]
	v_lshlrev_b32_e32 v34, 2, v36
	s_mov_b64 s[2:3], 0x480000
	v_lshl_add_u64 v[76:77], s[18:19], 0, v[34:35]
	s_movk_i32 s18, 0x90
	v_lshl_add_u64 v[70:71], v[42:43], 0, s[2:3]
	s_mov_b64 s[2:3], 0x4a0000
	v_lshl_add_u64 v[74:75], s[20:21], 0, v[34:35]
	v_mul_lo_u32 v35, v96, s18
	v_lshl_add_u64 v[72:73], v[42:43], 0, s[2:3]
	v_and_b32_e32 v42, 0x60, v184
	v_add3_u32 v98, 0, v35, v184
	v_lshlrev_b32_e32 v184, 1, v36
	v_lshlrev_b32_e32 v38, 2, v37
	v_cmp_gt_u32_e64 s[2:3], 2, v37
	v_lshlrev_b32_e32 v34, 3, v37
	v_mul_u32_u24_e32 v35, 0x110, v97
	v_mul_u32_u24_e32 v43, 0x90, v36
	v_lshl_add_u64 v[36:37], s[6:7], 0, v[184:185]
	s_mov_b64 s[6:7], 0x1000000
	v_lshl_add_u64 v[78:79], v[36:37], 0, s[6:7]
	v_lshlrev_b32_e32 v184, 1, v38
	v_lshlrev_b32_e32 v80, 1, v42
	s_lshl_b64 s[18:19], s[40:41], 2
	v_add_u32_e32 v101, v33, v35
	v_lshlrev_b32_e32 v86, 1, v34
	v_add_u32_e32 v102, v41, v43
	s_load_dwordx2 s[22:23], s[8:9], 0x38
	s_waitcnt lgkmcnt(0)
	s_add_u32 s22, s22, s18
	s_addc_u32 s23, s23, s19
	global_load_dwordx4 v[120:123], v185, s[22:23]
	s_branch .LBB0_310

.LBB0_310:
	s_and_b32 s27, s25, 0x7c0
	v_add_u32_e32 v88, s27, v96
	v_add_u32_e32 v34, s25, v96
	v_mov_b64_e32 v[32:33], s[10:11]
	v_mad_i64_i32 v[90:91], s[6:7], v34, s71, v[32:33]
	v_lshlrev_b32_e32 v32, 5, v88
	v_ashrrev_i32_e32 v33, 31, v32
	v_lshlrev_b64 v[36:37], 2, v[32:33]
	v_lshl_add_u64 v[32:33], v[66:67], 0, v[36:37]
	v_lshl_add_u64 v[36:37], v[68:69], 0, v[36:37]
	s_barrier
	global_load_dwordx4 v[32:35], v[32:33], off
	v_lshl_add_u64 v[40:41], v[90:91], 0, v[184:185]
	global_load_dwordx4 v[36:39], v[36:37], off
	v_add_co_u32_e32 v40, vcc, s86, v40
	v_mov_b32_e32 v81, v185
	s_nop 0
	v_addc_co_u32_e32 v41, vcc, 0, v41, vcc
	global_load_dwordx2 v[42:43], v[40:41], off offset:512
	global_load_dwordx2 v[44:45], v[40:41], off offset:576
	global_load_dwordx2 v[46:47], v[40:41], off offset:640
	global_load_dwordx2 v[48:49], v[40:41], off offset:704
	global_load_dwordx2 v[50:51], v[40:41], off offset:768
	global_load_dwordx2 v[52:53], v[40:41], off offset:832
	global_load_dwordx2 v[54:55], v[40:41], off offset:896
	global_load_dwordx2 v[56:57], v[40:41], off offset:960
	v_mov_b32_e32 v83, v185
	s_mov_b64 s[6:7], 0x1500
	v_lshlrev_b32_e32 v114, 4, v88
	v_ashrrev_i32_e32 v115, 31, v114
	v_lshlrev_b64 v[114:115], 2, v[114:115]
	v_lshl_add_u64 v[116:117], v[70:71], 0, v[114:115]
	v_lshl_add_u64 v[118:119], v[72:73], 0, v[114:115]
	v_lshl_add_u64 v[114:115], v[90:91], 0, v[80:81]
	global_load_dwordx4 v[124:127], v[116:117], off offset:16
	global_load_dwordx4 v[128:131], v[116:117], off
	v_lshl_add_u64 v[114:115], v[114:115], 0, v[82:83]
	global_load_dwordx4 v[132:135], v[118:119], off offset:16
	global_load_dwordx4 v[136:139], v[118:119], off
	v_lshl_add_u64 v[116:117], v[114:115], 0, s[6:7]
	v_lshl_add_u64 v[118:119], v[90:91], 0, v[82:83]
	s_mov_b64 s[20:21], 0x1600
	global_load_dwordx4 v[140:143], v[116:117], off
	global_load_dwordx4 v[144:147], v[116:117], off offset:32
	v_lshl_add_u64 v[118:119], v[118:119], 0, s[20:21]
	s_mov_b64 s[30:31], 0x1000
	s_add_i32 s20, s24, s25
	global_load_dwordx4 v[148:151], v[118:119], off
	global_load_dwordx4 v[152:155], v[118:119], off offset:32
	v_lshl_add_u64 v[116:117], v[90:91], 0, s[30:31]
	s_mul_i32 s21, s20, 0x1800
	s_mul_hi_i32 s23, s20, 0x1800
	s_add_u32 s22, s10, s21
	s_addc_u32 s23, s11, s23
	v_mov_b32_e32 v85, v185
	global_load_dwordx2 v[156:157], v[116:117], off offset:1608
	v_lshl_add_u64 v[118:119], s[22:23], 0, v[84:85]
	s_mov_b64 s[20:21], 0x1800
	v_lshl_add_u64 v[118:119], v[118:119], 0, s[30:31]
	global_load_dword v158, v[118:119], off offset:1024
	v_lshl_add_u64 v[118:119], v[118:119], 0, s[20:21]
	global_load_dword v159, v[118:119], off offset:1024
	v_lshl_add_u64 v[118:119], v[118:119], 0, s[20:21]
	global_load_dword v160, v[118:119], off offset:1024
	v_lshl_add_u64 v[118:119], v[118:119], 0, s[20:21]
	global_load_dword v161, v[118:119], off offset:1024
	v_lshl_add_u64 v[118:119], v[118:119], 0, s[20:21]
	global_load_dword v162, v[118:119], off offset:1024
	v_lshl_add_u64 v[118:119], v[118:119], 0, s[20:21]
	global_load_dword v163, v[118:119], off offset:1024
	v_lshl_add_u64 v[118:119], v[118:119], 0, s[20:21]
	global_load_dword v164, v[118:119], off offset:1024
	v_lshl_add_u64 v[118:119], v[118:119], 0, s[20:21]
	global_load_dword v165, v[118:119], off offset:1024
	s_waitcnt vmcnt(24)
	v_lshlrev_b32_e32 v58, 16, v42
	s_waitcnt vmcnt(23)
	v_lshlrev_b32_e32 v60, 16, v44
	v_and_b32_e32 v61, 0xffff0000, v44
	v_and_b32_e32 v59, 0xffff0000, v42
	v_pk_mul_f32 v[62:63], v[36:37], v[60:61]
	v_pk_mul_f32 v[60:61], v[32:33], v[60:61]
	v_pk_fma_f32 v[62:63], v[32:33], v[58:59], v[62:63] neg_lo:[0,0,1] neg_hi:[0,0,1]
	v_pk_fma_f32 v[58:59], v[36:37], v[58:59], v[60:61]
	v_lshlrev_b32_e32 v60, 16, v45
	v_and_b32_e32 v61, 0xffff0000, v45
	v_cvt_pk_bf16_f32 v42, v62, v63
	v_cvt_pk_bf16_f32 v44, v58, v59
	v_lshlrev_b32_e32 v58, 16, v43
	v_and_b32_e32 v59, 0xffff0000, v43
	v_pk_mul_f32 v[62:63], v[38:39], v[60:61]
	v_pk_mul_f32 v[60:61], v[34:35], v[60:61]
	v_pk_fma_f32 v[62:63], v[34:35], v[58:59], v[62:63] neg_lo:[0,0,1] neg_hi:[0,0,1]
	v_pk_fma_f32 v[58:59], v[38:39], v[58:59], v[60:61]
	v_cvt_pk_bf16_f32 v43, v62, v63
	v_cvt_pk_bf16_f32 v45, v58, v59
	global_store_dwordx2 v[40:41], v[42:43], off offset:512
	global_store_dwordx2 v[40:41], v[44:45], off offset:576
	s_waitcnt vmcnt(23)
	v_lshlrev_b32_e32 v44, 16, v48
	v_and_b32_e32 v45, 0xffff0000, v48
	v_lshlrev_b32_e32 v42, 16, v46
	v_and_b32_e32 v43, 0xffff0000, v46
	v_pk_mul_f32 v[58:59], v[36:37], v[44:45]
	v_pk_mul_f32 v[44:45], v[32:33], v[44:45]
	v_pk_fma_f32 v[58:59], v[32:33], v[42:43], v[58:59] neg_lo:[0,0,1] neg_hi:[0,0,1]
	v_lshlrev_b32_e32 v48, 16, v49
	v_and_b32_e32 v49, 0xffff0000, v49
	v_cvt_pk_bf16_f32 v46, v58, v59
	v_pk_fma_f32 v[42:43], v[36:37], v[42:43], v[44:45]
	v_lshlrev_b32_e32 v44, 16, v47
	v_and_b32_e32 v45, 0xffff0000, v47
	v_pk_mul_f32 v[58:59], v[38:39], v[48:49]
	v_pk_mul_f32 v[48:49], v[34:35], v[48:49]
	v_pk_fma_f32 v[58:59], v[34:35], v[44:45], v[58:59] neg_lo:[0,0,1] neg_hi:[0,0,1]
	v_pk_fma_f32 v[44:45], v[38:39], v[44:45], v[48:49]
	v_cvt_pk_bf16_f32 v42, v42, v43
	v_cvt_pk_bf16_f32 v47, v58, v59
	v_cvt_pk_bf16_f32 v43, v44, v45
	s_waitcnt vmcnt(21)
	v_lshlrev_b32_e32 v44, 16, v52
	v_and_b32_e32 v45, 0xffff0000, v52
	global_store_dwordx2 v[40:41], v[46:47], off offset:640
	global_store_dwordx2 v[40:41], v[42:43], off offset:704
	v_lshlrev_b32_e32 v42, 16, v50
	v_and_b32_e32 v43, 0xffff0000, v50
	v_pk_mul_f32 v[46:47], v[36:37], v[44:45]
	v_pk_mul_f32 v[44:45], v[32:33], v[44:45]
	v_lshlrev_b32_e32 v48, 16, v53
	v_and_b32_e32 v49, 0xffff0000, v53
	v_pk_fma_f32 v[46:47], v[32:33], v[42:43], v[46:47] neg_lo:[0,0,1] neg_hi:[0,0,1]
	v_pk_fma_f32 v[42:43], v[36:37], v[42:43], v[44:45]
	v_lshlrev_b32_e32 v44, 16, v51
	v_and_b32_e32 v45, 0xffff0000, v51
	v_pk_mul_f32 v[50:51], v[38:39], v[48:49]
	v_pk_mul_f32 v[48:49], v[34:35], v[48:49]
	v_pk_fma_f32 v[50:51], v[34:35], v[44:45], v[50:51] neg_lo:[0,0,1] neg_hi:[0,0,1]
	v_pk_fma_f32 v[44:45], v[38:39], v[44:45], v[48:49]
	v_cvt_pk_bf16_f32 v46, v46, v47
	v_cvt_pk_bf16_f32 v42, v42, v43
	v_cvt_pk_bf16_f32 v47, v50, v51
	v_cvt_pk_bf16_f32 v43, v44, v45
	s_waitcnt vmcnt(21)
	v_lshlrev_b32_e32 v44, 16, v56
	v_and_b32_e32 v45, 0xffff0000, v56
	global_store_dwordx2 v[40:41], v[46:47], off offset:768
	global_store_dwordx2 v[40:41], v[42:43], off offset:832
	v_lshlrev_b32_e32 v42, 16, v54
	v_and_b32_e32 v43, 0xffff0000, v54
	v_pk_mul_f32 v[46:47], v[36:37], v[44:45]
	v_lshl_add_u64 v[48:49], v[90:91], 0, v[80:81]
	v_pk_fma_f32 v[46:47], v[32:33], v[42:43], v[46:47] neg_lo:[0,0,1] neg_hi:[0,0,1]
	v_pk_mul_f32 v[32:33], v[32:33], v[44:45]
	v_cvt_pk_bf16_f32 v46, v46, v47
	v_pk_fma_f32 v[32:33], v[36:37], v[42:43], v[32:33]
	v_lshlrev_b32_e32 v42, 16, v57
	v_and_b32_e32 v43, 0xffff0000, v57
	v_lshlrev_b32_e32 v36, 16, v55
	v_and_b32_e32 v37, 0xffff0000, v55
	v_pk_mul_f32 v[44:45], v[38:39], v[42:43]
	v_cvt_pk_bf16_f32 v32, v32, v33
	v_pk_fma_f32 v[44:45], v[34:35], v[36:37], v[44:45] neg_lo:[0,0,1] neg_hi:[0,0,1]
	v_pk_mul_f32 v[34:35], v[34:35], v[42:43]
	v_cvt_pk_bf16_f32 v47, v44, v45
	v_pk_fma_f32 v[34:35], v[38:39], v[36:37], v[34:35]
	v_lshl_add_u64 v[48:49], v[48:49], 0, v[82:83]
	v_cvt_pk_bf16_f32 v33, v34, v35
	global_store_dwordx2 v[40:41], v[46:47], off offset:896
	global_store_dwordx2 v[40:41], v[32:33], off offset:960
	v_lshl_add_u64 v[94:95], v[48:49], 0, s[6:7]
	v_lshl_add_u64 v[50:51], v[90:91], 0, v[82:83]
	s_mov_b64 s[6:7], 0x1600
	s_nop 0
	v_lshl_add_u64 v[92:93], v[50:51], 0, s[6:7]
	s_waitcnt vmcnt(19)
	v_mov_b64_e32 v[32:33], v[124:125]
	v_mov_b64_e32 v[34:35], v[126:127]
	v_mov_b64_e32 v[40:41], v[128:129]
	v_mov_b64_e32 v[42:43], v[130:131]
	v_mov_b64_e32 v[36:37], v[132:133]
	v_mov_b64_e32 v[38:39], v[134:135]
	v_mov_b64_e32 v[44:45], v[136:137]
	v_mov_b64_e32 v[46:47], v[138:139]
	v_mov_b64_e32 v[48:49], v[140:141]
	v_mov_b64_e32 v[50:51], v[142:143]
	v_mov_b64_e32 v[52:53], v[144:145]
	v_mov_b64_e32 v[54:55], v[146:147]
	v_lshlrev_b32_e32 v106, 16, v52
	v_and_b32_e32 v107, 0xffff0000, v52
	v_lshlrev_b32_e32 v104, 16, v48
	v_and_b32_e32 v105, 0xffff0000, v48
	v_pk_mul_f32 v[108:109], v[44:45], v[106:107]
	v_pk_mul_f32 v[106:107], v[40:41], v[106:107]
	v_lshlrev_b32_e32 v52, 16, v53
	v_and_b32_e32 v53, 0xffff0000, v53
	v_pk_fma_f32 v[108:109], v[40:41], v[104:105], v[108:109] neg_lo:[0,0,1] neg_hi:[0,0,1]
	v_pk_fma_f32 v[104:105], v[44:45], v[104:105], v[106:107]
	v_lshlrev_b32_e32 v48, 16, v49
	v_and_b32_e32 v49, 0xffff0000, v49
	v_pk_mul_f32 v[106:107], v[46:47], v[52:53]
	v_pk_mul_f32 v[52:53], v[42:43], v[52:53]
	v_lshlrev_b32_e32 v110, 16, v54
	v_and_b32_e32 v111, 0xffff0000, v54
	v_pk_fma_f32 v[106:107], v[42:43], v[48:49], v[106:107] neg_lo:[0,0,1] neg_hi:[0,0,1]
	v_pk_fma_f32 v[52:53], v[46:47], v[48:49], v[52:53]
	v_lshlrev_b32_e32 v48, 16, v50
	v_and_b32_e32 v49, 0xffff0000, v50
	v_pk_mul_f32 v[112:113], v[36:37], v[110:111]
	v_pk_mul_f32 v[110:111], v[32:33], v[110:111]
	v_lshlrev_b32_e32 v54, 16, v55
	v_and_b32_e32 v55, 0xffff0000, v55
	v_pk_fma_f32 v[112:113], v[32:33], v[48:49], v[112:113] neg_lo:[0,0,1] neg_hi:[0,0,1]
	v_pk_fma_f32 v[110:111], v[36:37], v[48:49], v[110:111]
	v_cvt_pk_bf16_f32 v48, v104, v105
	v_cvt_pk_bf16_f32 v49, v52, v53
	v_lshlrev_b32_e32 v52, 16, v51
	v_and_b32_e32 v53, 0xffff0000, v51
	v_pk_mul_f32 v[104:105], v[38:39], v[54:55]
	v_pk_mul_f32 v[54:55], v[34:35], v[54:55]
	v_pk_fma_f32 v[104:105], v[34:35], v[52:53], v[104:105] neg_lo:[0,0,1] neg_hi:[0,0,1]
	v_pk_fma_f32 v[52:53], v[38:39], v[52:53], v[54:55]
	v_cvt_pk_bf16_f32 v54, v112, v113
	v_cvt_pk_bf16_f32 v51, v52, v53
	v_cvt_pk_bf16_f32 v52, v108, v109
	v_cvt_pk_bf16_f32 v53, v106, v107
	v_cvt_pk_bf16_f32 v55, v104, v105
	v_cvt_pk_bf16_f32 v50, v110, v111
	global_store_dwordx4 v[94:95], v[52:55], off
	global_store_dwordx4 v[94:95], v[48:51], off offset:32
	s_and_saveexec_b64 s[6:7], s[2:3]
	s_cbranch_execz .LBB0_314
	s_waitcnt vmcnt(19)
	v_mov_b64_e32 v[56:57], v[148:149]
	v_mov_b64_e32 v[58:59], v[150:151]
	v_mov_b64_e32 v[60:61], v[152:153]
	v_mov_b64_e32 v[62:63], v[154:155]
	v_lshlrev_b32_e32 v52, 16, v56
	v_and_b32_e32 v53, 0xffff0000, v56
	v_lshlrev_b32_e32 v50, 16, v60
	v_and_b32_e32 v51, 0xffff0000, v60
	v_pk_mul_f32 v[48:49], v[44:45], v[52:53]
	v_pk_mul_f32 v[44:45], v[44:45], v[50:51]
	v_pk_fma_f32 v[48:49], v[40:41], v[50:51], v[48:49]
	v_lshlrev_b32_e32 v50, 16, v57
	v_and_b32_e32 v51, 0xffff0000, v57
	v_pk_fma_f32 v[40:41], v[40:41], v[52:53], v[44:45] neg_lo:[0,0,1] neg_hi:[0,0,1]
	v_lshlrev_b32_e32 v44, 16, v61
	v_and_b32_e32 v45, 0xffff0000, v61
	v_pk_mul_f32 v[52:53], v[46:47], v[50:51]
	v_cvt_pk_bf16_f32 v40, v40, v41
	v_pk_fma_f32 v[52:53], v[42:43], v[44:45], v[52:53]
	v_pk_mul_f32 v[44:45], v[46:47], v[44:45]
	v_cvt_pk_bf16_f32 v48, v48, v49
	v_pk_fma_f32 v[42:43], v[42:43], v[50:51], v[44:45] neg_lo:[0,0,1] neg_hi:[0,0,1]
	v_lshlrev_b32_e32 v44, 16, v58
	v_cvt_pk_bf16_f32 v41, v42, v43
	v_lshlrev_b32_e32 v42, 16, v62
	v_and_b32_e32 v43, 0xffff0000, v62
	v_and_b32_e32 v45, 0xffff0000, v58
	v_pk_mul_f32 v[46:47], v[36:37], v[44:45]
	v_pk_mul_f32 v[36:37], v[36:37], v[42:43]
	v_pk_fma_f32 v[46:47], v[32:33], v[42:43], v[46:47]
	v_pk_fma_f32 v[32:33], v[32:33], v[44:45], v[36:37] neg_lo:[0,0,1] neg_hi:[0,0,1]
	v_lshlrev_b32_e32 v36, 16, v59
	v_and_b32_e32 v37, 0xffff0000, v59
	v_cvt_pk_bf16_f32 v42, v32, v33
	v_lshlrev_b32_e32 v32, 16, v63
	v_and_b32_e32 v33, 0xffff0000, v63
	v_pk_mul_f32 v[44:45], v[38:39], v[36:37]
	v_cvt_pk_bf16_f32 v49, v52, v53
	v_pk_fma_f32 v[44:45], v[34:35], v[32:33], v[44:45]
	v_pk_mul_f32 v[32:33], v[38:39], v[32:33]
	v_cvt_pk_bf16_f32 v50, v46, v47
	v_pk_fma_f32 v[32:33], v[34:35], v[36:37], v[32:33] neg_lo:[0,0,1] neg_hi:[0,0,1]
	v_cvt_pk_bf16_f32 v51, v44, v45
	v_cvt_pk_bf16_f32 v43, v32, v33
	global_store_dwordx4 v[92:93], v[40:43], off
	global_store_dwordx4 v[92:93], v[48:51], off offset:32
.LBB0_314:
	s_or_b64 exec, exec, s[6:7]
	s_ashr_i32 s28, s0, 5
	s_and_saveexec_b64 s[6:7], s[4:5]
	s_cbranch_execz .LBB0_316
	s_lshl_b32 s20, s28, 2
	s_mov_b32 s34, 0xbfb8aa3b
	v_ashrrev_i32_e32 v89, 31, v88
	s_ashr_i32 s21, s20, 31
	s_lshl_b64 s[30:31], s[20:21], 13
	s_waitcnt vmcnt(20)
	v_lshlrev_b32_e32 v34, 16, v156
	v_and_b32_e32 v36, 0xffff0000, v156
	v_add_f32_e32 v34, v120, v34
	v_min_f32_e32 v39, 0, v34
	v_mul_f32_e64 v34, |v34|, s34
	v_exp_f32_e32 v34, v34
	v_lshlrev_b32_e32 v37, 16, v157
	v_and_b32_e32 v38, 0xffff0000, v157
	v_lshl_add_u64 v[32:33], v[88:89], 2, s[16:17]
	v_add_f32_e32 v34, 1.0, v34
	v_log_f32_e32 v34, v34
	s_nop 0
	v_fmac_f32_e32 v39, 0xbf317218, v34
	v_lshl_add_u64 v[34:35], v[32:33], 0, s[30:31]
	global_store_dword v[34:35], v39, off
	s_or_b32 s30, s20, 1
	s_ashr_i32 s31, s30, 31
	s_lshl_b64 s[30:31], s[30:31], 13
	v_add_f32_e32 v34, v121, v36
	v_min_f32_e32 v36, 0, v34
	v_mul_f32_e64 v34, |v34|, s34
	v_exp_f32_e32 v34, v34
	s_nop 0
	v_add_f32_e32 v34, 1.0, v34
	v_log_f32_e32 v34, v34
	s_nop 0
	v_fmac_f32_e32 v36, 0xbf317218, v34
	v_lshl_add_u64 v[34:35], v[32:33], 0, s[30:31]
	global_store_dword v[34:35], v36, off
	s_or_b32 s30, s20, 2
	s_ashr_i32 s31, s30, 31
	s_lshl_b64 s[30:31], s[30:31], 13
	s_or_b32 s20, s20, 3
	s_ashr_i32 s21, s20, 31
	s_lshl_b64 s[20:21], s[20:21], 13
	v_add_f32_e32 v34, v122, v37
	v_min_f32_e32 v36, 0, v34
	v_mul_f32_e64 v34, |v34|, s34
	v_exp_f32_e32 v34, v34
	s_nop 0
	v_add_f32_e32 v34, 1.0, v34
	v_log_f32_e32 v34, v34
	s_nop 0
	v_fmac_f32_e32 v36, 0xbf317218, v34
	v_lshl_add_u64 v[34:35], v[32:33], 0, s[30:31]
	global_store_dword v[34:35], v36, off
	v_lshl_add_u64 v[32:33], v[32:33], 0, s[20:21]
	v_add_f32_e32 v34, v123, v38
	v_min_f32_e32 v35, 0, v34
	v_mul_f32_e64 v34, |v34|, s34
	v_exp_f32_e32 v34, v34
	s_nop 0
	v_add_f32_e32 v34, 1.0, v34
	v_log_f32_e32 v34, v34
	s_nop 0
	v_fmac_f32_e32 v35, 0xbf317218, v34
	global_store_dword v[32:33], v35, off
.LBB0_316:
	s_or_b64 exec, exec, s[6:7]
	v_mov_b32_e32 v85, v185
	v_mov_b32_e32 v48, v185
	s_waitcnt vmcnt(16)
	v_mov_b32_e32 v34, v158
	v_mov_b32_e32 v36, v159
	v_mov_b32_e32 v37, v160
	v_mov_b32_e32 v38, v161
	v_mov_b32_e32 v39, v162
	v_mov_b32_e32 v40, v163
	v_mov_b32_e32 v41, v164
	v_mov_b32_e32 v42, v165
	s_andn2_b64 vcc, exec, s[14:15]
	v_lshlrev_b32_e32 v32, 16, v34
	v_and_b32_e32 v33, 0xffff0000, v34
	v_pk_mul_f32 v[34:35], v[32:33], v[32:33]
	s_nop 0
	v_add_f32_e32 v34, v34, v35
	s_nop 1
	v_add_f32_dpp v34, v34, v34 row_shr:1 row_mask:0xf bank_mask:0xf bound_ctrl:1
	s_nop 1
	v_add_f32_dpp v34, v34, v34 row_shr:2 row_mask:0xf bank_mask:0xf bound_ctrl:1
	s_nop 1
	v_add_f32_dpp v34, v34, v34 row_shr:4 row_mask:0xf bank_mask:0xf bound_ctrl:1
	s_nop 1
	v_add_f32_dpp v34, v34, v34 row_shr:8 row_mask:0xf bank_mask:0xf bound_ctrl:1
	s_nop 0
	v_readlane_b32 s20, v34, 31
	v_readlane_b32 s21, v34, 63
	v_readlane_b32 s6, v34, 15
	v_readlane_b32 s7, v34, 47
	v_mov_b32_e32 v34, s20
	v_mov_b32_e32 v35, s21
	v_pk_add_f32 v[34:35], s[6:7], v[34:35]
	s_nop 0
	v_add_f32_e32 v34, v34, v35
	v_fmamk_f32 v34, v34, 0x3c000000, v252
	v_rsq_f32_e32 v34, v34
	s_nop 0
	v_pk_mul_f32 v[32:33], v[34:35], v[32:33] op_sel_hi:[0,1]
	v_pk_mul_f32 v[32:33], v[64:65], v[32:33]
	s_nop 0
	v_cvt_pk_bf16_f32 v43, v32, v33
	v_lshlrev_b32_e32 v32, 16, v36
	v_and_b32_e32 v33, 0xffff0000, v36
	v_pk_mul_f32 v[34:35], v[32:33], v[32:33]
	s_nop 0
	v_add_f32_e32 v34, v34, v35
	s_nop 1
	v_add_f32_dpp v34, v34, v34 row_shr:1 row_mask:0xf bank_mask:0xf bound_ctrl:1
	s_nop 1
	v_add_f32_dpp v34, v34, v34 row_shr:2 row_mask:0xf bank_mask:0xf bound_ctrl:1
	s_nop 1
	v_add_f32_dpp v34, v34, v34 row_shr:4 row_mask:0xf bank_mask:0xf bound_ctrl:1
	s_nop 1
	v_add_f32_dpp v34, v34, v34 row_shr:8 row_mask:0xf bank_mask:0xf bound_ctrl:1
	s_nop 0
	v_readlane_b32 s20, v34, 31
	v_readlane_b32 s21, v34, 63
	v_readlane_b32 s6, v34, 15
	v_readlane_b32 s7, v34, 47
	v_mov_b32_e32 v34, s20
	v_mov_b32_e32 v35, s21
	v_pk_add_f32 v[34:35], s[6:7], v[34:35]
	s_nop 0
	v_add_f32_e32 v34, v34, v35
	v_fmamk_f32 v34, v34, 0x3c000000, v252
	v_rsq_f32_e32 v34, v34
	s_nop 0
	v_pk_mul_f32 v[32:33], v[34:35], v[32:33] op_sel_hi:[0,1]
	v_pk_mul_f32 v[32:33], v[64:65], v[32:33]
	s_nop 0
	v_cvt_pk_bf16_f32 v32, v32, v33
	ds_write2_b32 v100, v43, v32 offset1:68
	v_lshlrev_b32_e32 v32, 16, v37
	v_and_b32_e32 v33, 0xffff0000, v37
	v_pk_mul_f32 v[34:35], v[32:33], v[32:33]
	v_add_u32_e32 v37, 0x400, v100
	v_add_f32_e32 v34, v34, v35
	s_nop 1
	v_add_f32_dpp v34, v34, v34 row_shr:1 row_mask:0xf bank_mask:0xf bound_ctrl:1
	s_nop 1
	v_add_f32_dpp v34, v34, v34 row_shr:2 row_mask:0xf bank_mask:0xf bound_ctrl:1
	s_nop 1
	v_add_f32_dpp v34, v34, v34 row_shr:4 row_mask:0xf bank_mask:0xf bound_ctrl:1
	s_nop 1
	v_add_f32_dpp v34, v34, v34 row_shr:8 row_mask:0xf bank_mask:0xf bound_ctrl:1
	s_nop 0
	v_readlane_b32 s20, v34, 31
	v_readlane_b32 s21, v34, 63
	v_readlane_b32 s6, v34, 15
	v_readlane_b32 s7, v34, 47
	v_mov_b32_e32 v34, s20
	v_mov_b32_e32 v35, s21
	v_pk_add_f32 v[34:35], s[6:7], v[34:35]
	s_nop 0
	v_add_f32_e32 v34, v34, v35
	v_fmamk_f32 v34, v34, 0x3c000000, v252
	v_rsq_f32_e32 v34, v34
	s_nop 0
	v_pk_mul_f32 v[32:33], v[34:35], v[32:33] op_sel_hi:[0,1]
	v_pk_mul_f32 v[32:33], v[64:65], v[32:33]
	s_nop 0
	v_cvt_pk_bf16_f32 v36, v32, v33
	v_lshlrev_b32_e32 v32, 16, v38
	v_and_b32_e32 v33, 0xffff0000, v38
	v_pk_mul_f32 v[34:35], v[32:33], v[32:33]
	s_nop 0
	v_add_f32_e32 v34, v34, v35
	s_nop 1
	v_add_f32_dpp v34, v34, v34 row_shr:1 row_mask:0xf bank_mask:0xf bound_ctrl:1
	s_nop 1
	v_add_f32_dpp v34, v34, v34 row_shr:2 row_mask:0xf bank_mask:0xf bound_ctrl:1
	s_nop 1
	v_add_f32_dpp v34, v34, v34 row_shr:4 row_mask:0xf bank_mask:0xf bound_ctrl:1
	s_nop 1
	v_add_f32_dpp v34, v34, v34 row_shr:8 row_mask:0xf bank_mask:0xf bound_ctrl:1
	s_nop 0
	v_readlane_b32 s20, v34, 31
	v_readlane_b32 s21, v34, 63
	v_readlane_b32 s6, v34, 15
	v_readlane_b32 s7, v34, 47
	v_mov_b32_e32 v34, s20
	v_mov_b32_e32 v35, s21
	v_pk_add_f32 v[34:35], s[6:7], v[34:35]
	s_nop 0
	v_add_f32_e32 v34, v34, v35
	v_fmamk_f32 v34, v34, 0x3c000000, v252
	v_rsq_f32_e32 v34, v34
	s_nop 0
	v_pk_mul_f32 v[32:33], v[34:35], v[32:33] op_sel_hi:[0,1]
	v_pk_mul_f32 v[32:33], v[64:65], v[32:33]
	s_nop 0
	v_cvt_pk_bf16_f32 v32, v32, v33
	ds_write2_b32 v100, v36, v32 offset0:136 offset1:204
	v_lshlrev_b32_e32 v32, 16, v39
	v_and_b32_e32 v33, 0xffff0000, v39
	v_pk_mul_f32 v[34:35], v[32:33], v[32:33]
	s_nop 0
	v_add_f32_e32 v34, v34, v35
	s_nop 1
	v_add_f32_dpp v34, v34, v34 row_shr:1 row_mask:0xf bank_mask:0xf bound_ctrl:1
	s_nop 1
	v_add_f32_dpp v34, v34, v34 row_shr:2 row_mask:0xf bank_mask:0xf bound_ctrl:1
	s_nop 1
	v_add_f32_dpp v34, v34, v34 row_shr:4 row_mask:0xf bank_mask:0xf bound_ctrl:1
	s_nop 1
	v_add_f32_dpp v34, v34, v34 row_shr:8 row_mask:0xf bank_mask:0xf bound_ctrl:1
	s_nop 0
	v_readlane_b32 s20, v34, 31
	v_readlane_b32 s21, v34, 63
	v_readlane_b32 s6, v34, 15
	v_readlane_b32 s7, v34, 47
	v_mov_b32_e32 v34, s20
	v_mov_b32_e32 v35, s21
	v_pk_add_f32 v[34:35], s[6:7], v[34:35]
	s_nop 0
	v_add_f32_e32 v34, v34, v35
	v_fmamk_f32 v34, v34, 0x3c000000, v252
	v_rsq_f32_e32 v34, v34
	s_nop 0
	v_pk_mul_f32 v[32:33], v[34:35], v[32:33] op_sel_hi:[0,1]
	v_pk_mul_f32 v[32:33], v[64:65], v[32:33]
	s_nop 0
	v_cvt_pk_bf16_f32 v36, v32, v33
	v_lshlrev_b32_e32 v32, 16, v40
	v_and_b32_e32 v33, 0xffff0000, v40
	v_pk_mul_f32 v[34:35], v[32:33], v[32:33]
	v_mov_b32_e32 v40, v185
	v_add_f32_e32 v34, v34, v35
	s_nop 1
	v_add_f32_dpp v34, v34, v34 row_shr:1 row_mask:0xf bank_mask:0xf bound_ctrl:1
	s_nop 1
	v_add_f32_dpp v34, v34, v34 row_shr:2 row_mask:0xf bank_mask:0xf bound_ctrl:1
	s_nop 1
	v_add_f32_dpp v34, v34, v34 row_shr:4 row_mask:0xf bank_mask:0xf bound_ctrl:1
	s_nop 1
	v_add_f32_dpp v34, v34, v34 row_shr:8 row_mask:0xf bank_mask:0xf bound_ctrl:1
	s_nop 0
	v_readlane_b32 s20, v34, 31
	v_readlane_b32 s21, v34, 63
	v_readlane_b32 s6, v34, 15
	v_readlane_b32 s7, v34, 47
	v_mov_b32_e32 v34, s20
	v_mov_b32_e32 v35, s21
	v_pk_add_f32 v[34:35], s[6:7], v[34:35]
	s_nop 0
	v_add_f32_e32 v34, v34, v35
	v_fmamk_f32 v34, v34, 0x3c000000, v252
	v_rsq_f32_e32 v34, v34
	s_nop 0
	v_pk_mul_f32 v[32:33], v[34:35], v[32:33] op_sel_hi:[0,1]
	v_pk_mul_f32 v[32:33], v[64:65], v[32:33]
	s_nop 0
	v_cvt_pk_bf16_f32 v32, v32, v33
	ds_write2_b32 v37, v36, v32 offset0:16 offset1:84
	v_lshlrev_b32_e32 v32, 16, v41
	v_and_b32_e32 v33, 0xffff0000, v41
	v_pk_mul_f32 v[34:35], v[32:33], v[32:33]
	s_nop 0
	v_add_f32_e32 v34, v34, v35
	s_nop 1
	v_add_f32_dpp v34, v34, v34 row_shr:1 row_mask:0xf bank_mask:0xf bound_ctrl:1
	s_nop 1
	v_add_f32_dpp v34, v34, v34 row_shr:2 row_mask:0xf bank_mask:0xf bound_ctrl:1
	s_nop 1
	v_add_f32_dpp v34, v34, v34 row_shr:4 row_mask:0xf bank_mask:0xf bound_ctrl:1
	s_nop 1
	v_add_f32_dpp v34, v34, v34 row_shr:8 row_mask:0xf bank_mask:0xf bound_ctrl:1
	s_nop 0
	v_readlane_b32 s20, v34, 31
	v_readlane_b32 s21, v34, 63
	v_readlane_b32 s6, v34, 15
	v_readlane_b32 s7, v34, 47
	v_mov_b32_e32 v34, s20
	v_mov_b32_e32 v35, s21
	v_pk_add_f32 v[34:35], s[6:7], v[34:35]
	s_nop 0
	v_add_f32_e32 v34, v34, v35
	v_fmamk_f32 v34, v34, 0x3c000000, v252
	v_rsq_f32_e32 v34, v34
	s_nop 0
	v_pk_mul_f32 v[32:33], v[34:35], v[32:33] op_sel_hi:[0,1]
	v_pk_mul_f32 v[32:33], v[64:65], v[32:33]
	s_nop 0
	v_cvt_pk_bf16_f32 v36, v32, v33
	v_lshlrev_b32_e32 v32, 16, v42
	v_and_b32_e32 v33, 0xffff0000, v42
	v_pk_mul_f32 v[34:35], v[32:33], v[32:33]
	s_nop 0
	v_add_f32_e32 v34, v34, v35
	s_nop 1
	v_add_f32_dpp v34, v34, v34 row_shr:1 row_mask:0xf bank_mask:0xf bound_ctrl:1
	s_nop 1
	v_add_f32_dpp v34, v34, v34 row_shr:2 row_mask:0xf bank_mask:0xf bound_ctrl:1
	s_nop 1
	v_add_f32_dpp v34, v34, v34 row_shr:4 row_mask:0xf bank_mask:0xf bound_ctrl:1
	s_nop 1
	v_add_f32_dpp v34, v34, v34 row_shr:8 row_mask:0xf bank_mask:0xf bound_ctrl:1
	s_nop 0
	v_readlane_b32 s20, v34, 31
	v_readlane_b32 s21, v34, 63
	v_readlane_b32 s6, v34, 15
	v_readlane_b32 s7, v34, 47
	v_mov_b32_e32 v34, s20
	v_mov_b32_e32 v35, s21
	v_pk_add_f32 v[34:35], s[6:7], v[34:35]
	s_mov_b64 s[20:21], -1
	v_add_f32_e32 v34, v34, v35
	v_fmamk_f32 v34, v34, 0x3c000000, v252
	v_rsq_f32_e32 v34, v34
	s_nop 0
	v_pk_mul_f32 v[32:33], v[34:35], v[32:33] op_sel_hi:[0,1]
	v_pk_mul_f32 v[32:33], v[64:65], v[32:33]
	s_nop 0
	v_cvt_pk_bf16_f32 v32, v32, v33
	ds_write2_b32 v37, v36, v32 offset0:152 offset1:220
	v_mov_b32_e32 v32, v185
	v_mov_b32_e32 v36, v185
	s_waitcnt lgkmcnt(0)
	s_barrier
	ds_read_b128 v[44:47], v101
	ds_read_b128 v[52:55], v101 offset:192
	v_mov_b32_e32 v33, v32
	v_mov_b32_e32 v34, v32
	v_mov_b32_e32 v35, v32
	v_mov_b32_e32 v41, v40
	v_mov_b32_e32 v42, v40
	v_mov_b32_e32 v43, v40
	s_waitcnt lgkmcnt(1)
	v_mfma_f32_16x16x32_bf16 v[32:35], v[28:31], v[44:47], v[32:35]
	v_mov_b32_e32 v37, v36
	v_mov_b32_e32 v38, v36
	v_mov_b32_e32 v39, v36
	v_mfma_f32_16x16x32_bf16 v[40:43], v[12:15], v[44:47], v[40:43]
	ds_read_b128 v[44:47], v101 offset:64
	v_mov_b32_e32 v49, v48
	v_mov_b32_e32 v50, v48
	s_waitcnt lgkmcnt(0)
	v_mfma_f32_16x16x32_bf16 v[32:35], v[24:27], v[44:47], v[32:35]
	v_mov_b32_e32 v51, v48
	v_mfma_f32_16x16x32_bf16 v[40:43], v[8:11], v[44:47], v[40:43]
	ds_read_b128 v[44:47], v101 offset:128
	s_waitcnt lgkmcnt(0)
	v_mfma_f32_16x16x32_bf16 v[32:35], v[20:23], v[44:47], v[32:35]
	v_mfma_f32_16x16x32_bf16 v[40:43], v[4:7], v[44:47], v[40:43]
	v_mfma_f32_16x16x32_bf16 v[44:47], v[16:19], v[52:55], v[32:35]
	s_nop 5
	ds_read_b128 v[32:35], v101 offset:4352
	s_waitcnt lgkmcnt(0)
	v_mfma_f32_16x16x32_bf16 v[36:39], v[28:31], v[32:35], v[36:39]
	v_mfma_f32_16x16x32_bf16 v[32:35], v[12:15], v[32:35], v[48:51]
	s_nop 2
	ds_read_b128 v[48:51], v101 offset:4416
	s_waitcnt lgkmcnt(0)
	v_mfma_f32_16x16x32_bf16 v[36:39], v[24:27], v[48:51], v[36:39]
	v_mfma_f32_16x16x32_bf16 v[32:35], v[8:11], v[48:51], v[32:35]
	ds_read_b128 v[48:51], v101 offset:4480
	s_waitcnt lgkmcnt(0)
	v_mfma_f32_16x16x32_bf16 v[36:39], v[20:23], v[48:51], v[36:39]
	v_mfma_f32_16x16x32_bf16 v[32:35], v[4:7], v[48:51], v[32:35]
	ds_read_b128 v[48:51], v101 offset:4544
	v_mfma_f32_16x16x32_bf16 v[40:43], v[0:3], v[52:55], v[40:43]
	s_waitcnt lgkmcnt(0)
	v_mfma_f32_16x16x32_bf16 v[36:39], v[16:19], v[48:51], v[36:39]
	v_mfma_f32_16x16x32_bf16 v[32:35], v[0:3], v[48:51], v[32:35]
	v_cndmask_b32_e64 v48, 0, 1, s[14:15]
	v_cmp_ne_u32_e64 s[6:7], 1, v48
	s_cbranch_vccnz .LBB0_320
	v_bfe_u32 v48, v44, 16, 1
	s_movk_i32 s20, 0x7fff
	v_add3_u32 v48, v44, v48, s20
	ds_write_b16_d16_hi v102, v48 offset:32768
	v_bfe_u32 v48, v45, 16, 1
	v_add3_u32 v48, v45, v48, s20
	ds_write_b16_d16_hi v102, v48 offset:32912
	v_bfe_u32 v48, v46, 16, 1
	v_add3_u32 v48, v46, v48, s20
	ds_write_b16_d16_hi v102, v48 offset:33056
	v_bfe_u32 v48, v47, 16, 1
	v_add3_u32 v48, v47, v48, s20
	ds_write_b16_d16_hi v102, v48 offset:33200
	v_bfe_u32 v48, v40, 16, 1
	v_add3_u32 v48, v40, v48, s20
	ds_write_b16_d16_hi v102, v48 offset:37376
	v_bfe_u32 v48, v41, 16, 1
	v_add3_u32 v48, v41, v48, s20
	ds_write_b16_d16_hi v102, v48 offset:37520
	v_bfe_u32 v48, v42, 16, 1
	v_add3_u32 v48, v42, v48, s20
	ds_write_b16_d16_hi v102, v48 offset:37664
	v_bfe_u32 v48, v43, 16, 1
	v_add3_u32 v48, v43, v48, s20
	ds_write_b16_d16_hi v102, v48 offset:37808
	s_cbranch_execz .LBB0_321
